# fp8 packing in the expert GEMM2 epilogues: 62 dead zero initialisers removed (on top of v76)
# speedup vs baseline: 1.0043x; 1.0043x over previous
.LBB0_1122:
	s_lshl_b32 s2, s87, 7
	v_add_u32_e32 v142, s80, v205
	v_add_u32_e32 v158, s81, v205
	s_add_u32 s64, s38, s2
	ds_read_b128 v[130:133], v142
	ds_read_b128 v[134:137], v142 offset:1024
	ds_read_b128 v[138:141], v142 offset:2048
	ds_read_b128 v[142:145], v142 offset:3072
	ds_read_b128 v[146:149], v158
	ds_read_b128 v[150:153], v158 offset:1024
	ds_read_b128 v[154:157], v158 offset:2048
	ds_read_b128 v[158:161], v158 offset:3072
	s_addc_u32 s65, s39, 0
	s_add_u32 s66, s64, 0x100
	s_addc_u32 s67, s65, 0
	s_and_b64 s[64:65], s[60:61], exec
	s_cselect_b32 s65, s35, s67
	s_cselect_b32 s64, s83, s66
	s_add_i32 s68, s2, 0x100
	s_and_b64 s[66:67], s[60:61], exec
	s_cselect_b32 s68, 0, s68
	s_add_u32 s2, s36, s2
	s_addc_u32 s67, s37, 0
	s_add_u32 s66, s2, 0x20080
	s_addc_u32 s67, s67, 0
	v_lshl_add_u64 v[210:211], s[66:67], 0, v[194:195]
	s_add_i32 m0, s50, 0xc000
	ds_read_b128 v[162:165], v209
	ds_read_b128 v[166:169], v209 offset:1024
	ds_read_b128 v[170:173], v209 offset:2048
	ds_read_b128 v[174:177], v209 offset:3072
	ds_read_b128 v[178:181], v209 offset:4096
	ds_read_b128 v[182:185], v209 offset:5120
	ds_read_b128 v[186:189], v209 offset:6144
	ds_read_b128 v[190:193], v209 offset:7168
	global_load_lds_dwordx4 v[210:211], off
	v_lshl_add_u64 v[210:211], s[66:67], 0, v[198:199]
	s_add_i32 m0, s50, 0xe000
	s_nop 0
	global_load_lds_dwordx4 v[210:211], off
	s_waitcnt vmcnt(8)
	s_waitcnt lgkmcnt(0)
	s_barrier
	s_waitcnt lgkmcnt(0)
	v_mfma_f32_16x16x32_bf16 v[86:89], v[130:133], v[162:165], v[86:89]
	v_mfma_f32_16x16x32_bf16 v[82:85], v[138:141], v[162:165], v[82:85]
	v_mfma_f32_16x16x32_bf16 v[78:81], v[130:133], v[170:173], v[78:81]
	v_mfma_f32_16x16x32_bf16 v[74:77], v[138:141], v[170:173], v[74:77]
	v_mfma_f32_16x16x32_bf16 v[70:73], v[130:133], v[178:181], v[70:73]
	v_mfma_f32_16x16x32_bf16 v[66:69], v[138:141], v[178:181], v[66:69]
	v_mfma_f32_16x16x32_bf16 v[62:65], v[130:133], v[186:189], v[62:65]
	v_mfma_f32_16x16x32_bf16 v[58:61], v[138:141], v[186:189], v[58:61]
	v_mfma_f32_16x16x32_bf16 v[86:89], v[134:137], v[166:169], v[86:89]
	v_mfma_f32_16x16x32_bf16 v[82:85], v[142:145], v[166:169], v[82:85]
	v_mfma_f32_16x16x32_bf16 v[78:81], v[134:137], v[174:177], v[78:81]
	v_mfma_f32_16x16x32_bf16 v[74:77], v[142:145], v[174:177], v[74:77]
	v_mfma_f32_16x16x32_bf16 v[70:73], v[134:137], v[182:185], v[70:73]
	v_mfma_f32_16x16x32_bf16 v[66:69], v[142:145], v[182:185], v[66:69]
	v_mfma_f32_16x16x32_bf16 v[62:65], v[134:137], v[190:193], v[62:65]
	v_mfma_f32_16x16x32_bf16 v[58:61], v[142:145], v[190:193], v[58:61]
	v_mfma_f32_16x16x32_bf16 v[54:57], v[146:149], v[162:165], v[54:57]
	v_mfma_f32_16x16x32_bf16 v[50:53], v[154:157], v[162:165], v[50:53]
	v_mfma_f32_16x16x32_bf16 v[46:49], v[146:149], v[170:173], v[46:49]
	v_mfma_f32_16x16x32_bf16 v[42:45], v[154:157], v[170:173], v[42:45]
	v_mfma_f32_16x16x32_bf16 v[34:37], v[146:149], v[178:181], v[34:37]
	v_mfma_f32_16x16x32_bf16 v[26:29], v[154:157], v[178:181], v[26:29]
	v_mfma_f32_16x16x32_bf16 v[18:21], v[146:149], v[186:189], v[18:21]
	v_mfma_f32_16x16x32_bf16 v[10:13], v[154:157], v[186:189], v[10:13]
	v_mfma_f32_16x16x32_bf16 v[54:57], v[150:153], v[166:169], v[54:57]
	v_mfma_f32_16x16x32_bf16 v[50:53], v[158:161], v[166:169], v[50:53]
	v_mfma_f32_16x16x32_bf16 v[46:49], v[150:153], v[174:177], v[46:49]
	v_mfma_f32_16x16x32_bf16 v[42:45], v[158:161], v[174:177], v[42:45]
	v_mfma_f32_16x16x32_bf16 v[34:37], v[150:153], v[182:185], v[34:37]
	v_mfma_f32_16x16x32_bf16 v[26:29], v[158:161], v[182:185], v[26:29]
	v_mfma_f32_16x16x32_bf16 v[18:21], v[150:153], v[190:193], v[18:21]
	v_mfma_f32_16x16x32_bf16 v[10:13], v[158:161], v[190:193], v[10:13]
	s_barrier
	s_add_i32 s2, s80, s49
	v_lshl_add_u64 v[210:211], s[64:65], 0, v[196:197]
	s_mov_b32 m0, s2
	ds_read_b128 v[162:165], v209 offset:16384
	ds_read_b128 v[166:169], v209 offset:17408
	ds_read_b128 v[170:173], v209 offset:18432
	ds_read_b128 v[174:177], v209 offset:19456
	ds_read_b128 v[178:181], v209 offset:20480
	ds_read_b128 v[182:185], v209 offset:21504
	ds_read_b128 v[186:189], v209 offset:22528
	ds_read_b128 v[190:193], v209 offset:23552
	global_load_lds_dwordx4 v[210:211], off
	s_add_i32 m0, s2, 0x2000
	s_add_u32 s66, s64, 0x20000
	v_lshl_add_u64 v[212:213], s[64:65], 0, v[200:201]
	s_addc_u32 s67, s65, 0
	s_add_i32 s2, s81, s49
	global_load_lds_dwordx4 v[212:213], off
	v_lshl_add_u64 v[214:215], s[66:67], 0, v[196:197]
	s_mov_b32 m0, s2
	s_nop 0
	global_load_lds_dwordx4 v[214:215], off
	s_add_i32 m0, s2, 0x2000
	s_add_u32 s62, s62, s68
	v_lshl_add_u64 v[214:215], s[66:67], 0, v[200:201]
	s_addc_u32 s63, s63, 0
	global_load_lds_dwordx4 v[214:215], off
	v_lshl_add_u64 v[214:215], s[62:63], 0, v[194:195]
	s_mov_b32 m0, s50
	v_lshl_add_u64 v[216:217], s[62:63], 0, v[198:199]
	global_load_lds_dwordx4 v[214:215], off
	s_mov_b32 m0, s51
	s_nop 0
	global_load_lds_dwordx4 v[216:217], off
	s_waitcnt vmcnt(8)
	s_waitcnt lgkmcnt(0)
	s_barrier
	s_waitcnt lgkmcnt(0)
	v_mfma_f32_16x16x32_bf16 v[126:129], v[130:133], v[162:165], v[126:129]
	v_mfma_f32_16x16x32_bf16 v[122:125], v[138:141], v[162:165], v[122:125]
	v_mfma_f32_16x16x32_bf16 v[110:113], v[130:133], v[170:173], v[110:113]
	v_mfma_f32_16x16x32_bf16 v[106:109], v[138:141], v[170:173], v[106:109]
	v_mfma_f32_16x16x32_bf16 v[94:97], v[130:133], v[178:181], v[94:97]
	v_mfma_f32_16x16x32_bf16 v[90:93], v[138:141], v[178:181], v[90:93]
	v_mfma_f32_16x16x32_bf16 v[22:25], v[130:133], v[186:189], v[22:25]
	v_mfma_f32_16x16x32_bf16 v[14:17], v[138:141], v[186:189], v[14:17]
	v_mfma_f32_16x16x32_bf16 v[126:129], v[134:137], v[166:169], v[126:129]
	v_mfma_f32_16x16x32_bf16 v[122:125], v[142:145], v[166:169], v[122:125]
	v_mfma_f32_16x16x32_bf16 v[110:113], v[134:137], v[174:177], v[110:113]
	v_mfma_f32_16x16x32_bf16 v[106:109], v[142:145], v[174:177], v[106:109]
	v_mfma_f32_16x16x32_bf16 v[94:97], v[134:137], v[182:185], v[94:97]
	v_mfma_f32_16x16x32_bf16 v[90:93], v[142:145], v[182:185], v[90:93]
	v_mfma_f32_16x16x32_bf16 v[22:25], v[134:137], v[190:193], v[22:25]
	v_mfma_f32_16x16x32_bf16 v[14:17], v[142:145], v[190:193], v[14:17]
	v_mfma_f32_16x16x32_bf16 v[118:121], v[146:149], v[162:165], v[118:121]
	v_mfma_f32_16x16x32_bf16 v[114:117], v[154:157], v[162:165], v[114:117]
	v_mfma_f32_16x16x32_bf16 v[102:105], v[146:149], v[170:173], v[102:105]
	v_mfma_f32_16x16x32_bf16 v[98:101], v[154:157], v[170:173], v[98:101]
	v_mfma_f32_16x16x32_bf16 v[38:41], v[146:149], v[178:181], v[38:41]
	v_mfma_f32_16x16x32_bf16 v[30:33], v[154:157], v[178:181], v[30:33]
	v_mfma_f32_16x16x32_bf16 v[6:9], v[146:149], v[186:189], v[6:9]
	v_mfma_f32_16x16x32_bf16 v[2:5], v[154:157], v[186:189], v[2:5]
	v_mfma_f32_16x16x32_bf16 v[118:121], v[150:153], v[166:169], v[118:121]
	v_mfma_f32_16x16x32_bf16 v[114:117], v[158:161], v[166:169], v[114:117]
	v_mfma_f32_16x16x32_bf16 v[102:105], v[150:153], v[174:177], v[102:105]
	v_mfma_f32_16x16x32_bf16 v[98:101], v[158:161], v[174:177], v[98:101]
	v_mfma_f32_16x16x32_bf16 v[38:41], v[150:153], v[182:185], v[38:41]
	v_mfma_f32_16x16x32_bf16 v[30:33], v[158:161], v[182:185], v[30:33]
	v_mfma_f32_16x16x32_bf16 v[6:9], v[150:153], v[190:193], v[6:9]
	v_mfma_f32_16x16x32_bf16 v[2:5], v[158:161], v[190:193], v[2:5]
	s_barrier
	s_add_i32 s2, 0, 0x18000
	s_add_i32 s66, 0, 0x1c000
	v_add_u32_e32 v130, s2, v205
	v_add_u32_e32 v142, s66, v205
	ds_read_b128 v[146:149], v130
	ds_read_b128 v[150:153], v130 offset:1024
	ds_read_b128 v[154:157], v130 offset:2048
	ds_read_b128 v[158:161], v130 offset:3072
	ds_read_b128 v[130:133], v142
	ds_read_b128 v[134:137], v142 offset:1024
	ds_read_b128 v[138:141], v142 offset:2048
	ds_read_b128 v[142:145], v142 offset:3072
	s_add_u32 s62, s62, 0x20000
	s_addc_u32 s63, s63, 0
	s_mov_b32 m0, s52
	v_lshl_add_u64 v[218:219], s[62:63], 0, v[194:195]
	ds_read_b128 v[162:165], v209 offset:32768
	ds_read_b128 v[166:169], v209 offset:33792
	ds_read_b128 v[170:173], v209 offset:34816
	ds_read_b128 v[174:177], v209 offset:35840
	ds_read_b128 v[178:181], v209 offset:36864
	ds_read_b128 v[182:185], v209 offset:37888
	ds_read_b128 v[186:189], v209 offset:38912
	ds_read_b128 v[190:193], v209 offset:39936
	global_load_lds_dwordx4 v[218:219], off
	v_lshl_add_u64 v[218:219], s[62:63], 0, v[198:199]
	s_mov_b32 m0, s53
	s_nop 0
	global_load_lds_dwordx4 v[218:219], off
	s_waitcnt vmcnt(8)
	s_waitcnt lgkmcnt(0)
	s_barrier
	s_waitcnt lgkmcnt(0)
	v_mfma_f32_16x16x32_bf16 v[86:89], v[146:149], v[162:165], v[86:89]
	v_mfma_f32_16x16x32_bf16 v[82:85], v[154:157], v[162:165], v[82:85]
	v_mfma_f32_16x16x32_bf16 v[78:81], v[146:149], v[170:173], v[78:81]
	v_mfma_f32_16x16x32_bf16 v[74:77], v[154:157], v[170:173], v[74:77]
	v_mfma_f32_16x16x32_bf16 v[70:73], v[146:149], v[178:181], v[70:73]
	v_mfma_f32_16x16x32_bf16 v[66:69], v[154:157], v[178:181], v[66:69]
	v_mfma_f32_16x16x32_bf16 v[62:65], v[146:149], v[186:189], v[62:65]
	v_mfma_f32_16x16x32_bf16 v[58:61], v[154:157], v[186:189], v[58:61]
	v_mfma_f32_16x16x32_bf16 v[86:89], v[150:153], v[166:169], v[86:89]
	v_mfma_f32_16x16x32_bf16 v[82:85], v[158:161], v[166:169], v[82:85]
	v_mfma_f32_16x16x32_bf16 v[78:81], v[150:153], v[174:177], v[78:81]
	v_mfma_f32_16x16x32_bf16 v[74:77], v[158:161], v[174:177], v[74:77]
	v_mfma_f32_16x16x32_bf16 v[70:73], v[150:153], v[182:185], v[70:73]
	v_mfma_f32_16x16x32_bf16 v[66:69], v[158:161], v[182:185], v[66:69]
	v_mfma_f32_16x16x32_bf16 v[62:65], v[150:153], v[190:193], v[62:65]
	v_mfma_f32_16x16x32_bf16 v[58:61], v[158:161], v[190:193], v[58:61]
	v_mfma_f32_16x16x32_bf16 v[54:57], v[130:133], v[162:165], v[54:57]
	v_mfma_f32_16x16x32_bf16 v[50:53], v[138:141], v[162:165], v[50:53]
	v_mfma_f32_16x16x32_bf16 v[46:49], v[130:133], v[170:173], v[46:49]
	v_mfma_f32_16x16x32_bf16 v[42:45], v[138:141], v[170:173], v[42:45]
	v_mfma_f32_16x16x32_bf16 v[34:37], v[130:133], v[178:181], v[34:37]
	v_mfma_f32_16x16x32_bf16 v[26:29], v[138:141], v[178:181], v[26:29]
	v_mfma_f32_16x16x32_bf16 v[18:21], v[130:133], v[186:189], v[18:21]
	v_mfma_f32_16x16x32_bf16 v[10:13], v[138:141], v[186:189], v[10:13]
	v_mfma_f32_16x16x32_bf16 v[54:57], v[134:137], v[166:169], v[54:57]
	v_mfma_f32_16x16x32_bf16 v[50:53], v[142:145], v[166:169], v[50:53]
	v_mfma_f32_16x16x32_bf16 v[46:49], v[134:137], v[174:177], v[46:49]
	v_mfma_f32_16x16x32_bf16 v[42:45], v[142:145], v[174:177], v[42:45]
	v_mfma_f32_16x16x32_bf16 v[34:37], v[134:137], v[182:185], v[34:37]
	v_mfma_f32_16x16x32_bf16 v[26:29], v[142:145], v[182:185], v[26:29]
	v_mfma_f32_16x16x32_bf16 v[18:21], v[134:137], v[190:193], v[18:21]
	v_mfma_f32_16x16x32_bf16 v[10:13], v[142:145], v[190:193], v[10:13]
	s_barrier
	s_add_i32 s2, s2, s49
	v_lshl_add_u64 v[210:211], v[210:211], 0, s[12:13]
	s_mov_b32 m0, s2
	ds_read_b128 v[186:189], v209 offset:49152
	ds_read_b128 v[190:193], v209 offset:50176
	ds_read_b128 v[178:181], v209 offset:51200
	ds_read_b128 v[182:185], v209 offset:52224
	ds_read_b128 v[170:173], v209 offset:53248
	ds_read_b128 v[174:177], v209 offset:54272
	ds_read_b128 v[162:165], v209 offset:55296
	ds_read_b128 v[166:169], v209 offset:56320
	global_load_lds_dwordx4 v[210:211], off
	s_add_i32 m0, s2, 0x2000
	s_add_u32 s62, s64, 0x20080
	v_lshl_add_u64 v[210:211], v[212:213], 0, s[12:13]
	s_addc_u32 s63, s65, 0
	s_add_i32 s2, s66, s49
	global_load_lds_dwordx4 v[210:211], off
	v_lshl_add_u64 v[210:211], s[62:63], 0, v[196:197]
	s_mov_b32 m0, s2
	s_andn2_b64 vcc, exec, s[60:61]
	global_load_lds_dwordx4 v[210:211], off
	v_lshl_add_u64 v[210:211], s[62:63], 0, v[200:201]
	s_add_i32 m0, s2, 0x2000
	s_nop 0
	global_load_lds_dwordx4 v[210:211], off
	v_lshl_add_u64 v[210:211], v[214:215], 0, s[12:13]
	s_mov_b32 m0, s73
	s_nop 0
	global_load_lds_dwordx4 v[210:211], off
	v_lshl_add_u64 v[210:211], v[216:217], 0, s[12:13]
	s_mov_b32 m0, s74
	s_nop 0
	global_load_lds_dwordx4 v[210:211], off
	s_waitcnt vmcnt(8)
	s_waitcnt lgkmcnt(0)
	s_barrier
	s_cbranch_vccnz .LBB0_1104
	v_pk_mul_f32 v[214:215], v[86:87], s[20:21] op_sel_hi:[1,0]
	v_pk_mul_f32 v[216:217], v[82:83], s[20:21] op_sel_hi:[1,0]
	v_cvt_pk_fp8_f32 v218, v214, v215
	v_cvt_pk_fp8_f32 v219, v216, v217
	v_pk_mul_f32 v[214:215], v[88:89], s[20:21] op_sel_hi:[1,0]
	v_pk_mul_f32 v[216:217], v[84:85], s[20:21] op_sel_hi:[1,0]
	v_cvt_pk_fp8_f32 v218, v214, v215 op_sel:[0,0,1]
	v_cvt_pk_fp8_f32 v219, v216, v217 op_sel:[0,0,1]
	v_pk_mul_f32 v[214:215], v[54:55], s[20:21] op_sel_hi:[1,0]
	v_pk_mul_f32 v[216:217], v[50:51], s[20:21] op_sel_hi:[1,0]
	v_mov_b32_e32 v210, v1
	v_mov_b32_e32 v211, v204
	v_cvt_pk_fp8_f32 v220, v214, v215
	v_cvt_pk_fp8_f32 v221, v216, v217
	v_pk_mul_f32 v[214:215], v[56:57], s[20:21] op_sel_hi:[1,0]
	v_add_u32_e32 v210, s85, v210
	v_lshl_add_u32 v212, v211, 3, s86
	v_ashrrev_i32_e32 v211, 31, v210
	v_pk_mul_f32 v[216:217], v[52:53], s[20:21] op_sel_hi:[1,0]
	v_lshlrev_b64 v[210:211], 11, v[210:211]
	v_cvt_pk_fp8_f32 v220, v214, v215 op_sel:[0,0,1]
	v_cvt_pk_fp8_f32 v221, v216, v217 op_sel:[0,0,1]
	v_ashrrev_i32_e32 v213, 31, v212
	v_lshl_add_u64 v[210:211], s[10:11], 0, v[210:211]
	v_lshl_add_u64 v[210:211], v[210:211], 0, v[212:213]
	s_nop 1
	v_permlane16_swap_b32 v218, v220
	v_permlane16_swap_b32 v219, v221
	v_and_b32_e32 v216, 1, v204
	v_mul_u32_u24_e32 v216, 0x78, v216
	v_mov_b32_e32 v217, 0
	v_lshl_add_u64 v[216:217], v[210:211], 0, v[216:217]
	global_store_dwordx4 v[216:217], v[218:221], off
	v_pk_mul_f32 v[214:215], v[78:79], s[20:21] op_sel_hi:[1,0]
	v_pk_mul_f32 v[216:217], v[74:75], s[20:21] op_sel_hi:[1,0]
	v_cvt_pk_fp8_f32 v218, v214, v215
	v_cvt_pk_fp8_f32 v219, v216, v217
	v_pk_mul_f32 v[214:215], v[80:81], s[20:21] op_sel_hi:[1,0]
	v_pk_mul_f32 v[216:217], v[76:77], s[20:21] op_sel_hi:[1,0]
	v_cvt_pk_fp8_f32 v218, v214, v215 op_sel:[0,0,1]
	v_cvt_pk_fp8_f32 v219, v216, v217 op_sel:[0,0,1]
	v_pk_mul_f32 v[214:215], v[46:47], s[20:21] op_sel_hi:[1,0]
	v_pk_mul_f32 v[216:217], v[42:43], s[20:21] op_sel_hi:[1,0]
	v_cvt_pk_fp8_f32 v220, v214, v215
	v_cvt_pk_fp8_f32 v221, v216, v217
	v_pk_mul_f32 v[214:215], v[48:49], s[20:21] op_sel_hi:[1,0]
	v_pk_mul_f32 v[216:217], v[44:45], s[20:21] op_sel_hi:[1,0]
	v_cvt_pk_fp8_f32 v220, v214, v215 op_sel:[0,0,1]
	v_cvt_pk_fp8_f32 v221, v216, v217 op_sel:[0,0,1]
	s_mov_b32 s2, 0x8000
	v_add_co_u32_e32 v214, vcc, s2, v210
	s_mov_b64 s[60:61], 0x8000
	s_nop 0
	v_addc_co_u32_e32 v215, vcc, 0, v211, vcc
	v_lshl_add_u64 v[212:213], v[210:211], 0, s[60:61]
	s_nop 1
	v_permlane16_swap_b32 v218, v220
	v_permlane16_swap_b32 v219, v221
	v_and_b32_e32 v216, 1, v204
	v_mul_u32_u24_e32 v216, 0x78, v216
	v_mov_b32_e32 v217, 0
	v_lshl_add_u64 v[216:217], v[214:215], 0, v[216:217]
	global_store_dwordx4 v[216:217], v[218:221], off
	v_pk_mul_f32 v[214:215], v[70:71], s[20:21] op_sel_hi:[1,0]
	v_pk_mul_f32 v[216:217], v[66:67], s[20:21] op_sel_hi:[1,0]
	v_cvt_pk_fp8_f32 v218, v214, v215
	v_cvt_pk_fp8_f32 v219, v216, v217
	v_pk_mul_f32 v[214:215], v[72:73], s[20:21] op_sel_hi:[1,0]
	v_pk_mul_f32 v[216:217], v[68:69], s[20:21] op_sel_hi:[1,0]
	v_cvt_pk_fp8_f32 v218, v214, v215 op_sel:[0,0,1]
	v_cvt_pk_fp8_f32 v219, v216, v217 op_sel:[0,0,1]
	v_pk_mul_f32 v[214:215], v[34:35], s[20:21] op_sel_hi:[1,0]
	v_pk_mul_f32 v[216:217], v[26:27], s[20:21] op_sel_hi:[1,0]
	v_cvt_pk_fp8_f32 v220, v214, v215
	v_cvt_pk_fp8_f32 v221, v216, v217
	v_pk_mul_f32 v[214:215], v[36:37], s[20:21] op_sel_hi:[1,0]
	v_pk_mul_f32 v[216:217], v[28:29], s[20:21] op_sel_hi:[1,0]
	v_cvt_pk_fp8_f32 v220, v214, v215 op_sel:[0,0,1]
	v_cvt_pk_fp8_f32 v221, v216, v217 op_sel:[0,0,1]
	s_mov_b32 s2, 0x10000
	v_add_co_u32_e32 v214, vcc, s2, v210
	v_lshl_add_u64 v[212:213], v[210:211], 0, s[24:25]
	s_nop 0
	v_addc_co_u32_e32 v215, vcc, 0, v211, vcc
	s_nop 1
	v_permlane16_swap_b32 v218, v220
	v_permlane16_swap_b32 v219, v221
	v_and_b32_e32 v216, 1, v204
	v_mul_u32_u24_e32 v216, 0x78, v216
	v_mov_b32_e32 v217, 0
	v_lshl_add_u64 v[216:217], v[214:215], 0, v[216:217]
	global_store_dwordx4 v[216:217], v[218:221], off
	v_pk_mul_f32 v[214:215], v[62:63], s[20:21] op_sel_hi:[1,0]
	v_pk_mul_f32 v[216:217], v[58:59], s[20:21] op_sel_hi:[1,0]
	v_cvt_pk_fp8_f32 v218, v214, v215
	v_cvt_pk_fp8_f32 v219, v216, v217
	v_pk_mul_f32 v[214:215], v[64:65], s[20:21] op_sel_hi:[1,0]
	v_pk_mul_f32 v[216:217], v[60:61], s[20:21] op_sel_hi:[1,0]
	v_cvt_pk_fp8_f32 v218, v214, v215 op_sel:[0,0,1]
	v_cvt_pk_fp8_f32 v219, v216, v217 op_sel:[0,0,1]
	v_pk_mul_f32 v[214:215], v[18:19], s[20:21] op_sel_hi:[1,0]
	v_pk_mul_f32 v[216:217], v[10:11], s[20:21] op_sel_hi:[1,0]
	v_cvt_pk_fp8_f32 v220, v214, v215
	v_cvt_pk_fp8_f32 v221, v216, v217
	v_pk_mul_f32 v[214:215], v[20:21], s[20:21] op_sel_hi:[1,0]
	v_pk_mul_f32 v[216:217], v[12:13], s[20:21] op_sel_hi:[1,0]
	v_cvt_pk_fp8_f32 v220, v214, v215 op_sel:[0,0,1]
	v_cvt_pk_fp8_f32 v221, v216, v217 op_sel:[0,0,1]
	s_mov_b32 s2, 0x18000
	v_lshl_add_u64 v[212:213], v[210:211], 0, s[28:29]
	v_add_co_u32_e32 v210, vcc, s2, v210
	s_nop 1
	v_addc_co_u32_e32 v211, vcc, 0, v211, vcc
	s_nop 1
	v_permlane16_swap_b32 v218, v220
	v_permlane16_swap_b32 v219, v221
	v_and_b32_e32 v216, 1, v204
	v_mul_u32_u24_e32 v216, 0x78, v216
	v_mov_b32_e32 v217, 0
	v_lshl_add_u64 v[216:217], v[210:211], 0, v[216:217]
	global_store_dwordx4 v[216:217], v[218:221], off
	s_branch .LBB0_1104

.LBB0_1126:
	v_pk_mul_f32 v[20:21], v[126:127], s[20:21] op_sel_hi:[1,0]
	v_pk_mul_f32 v[26:27], v[122:123], s[20:21] op_sel_hi:[1,0]
	v_cvt_pk_fp8_f32 v42, v20, v21
	v_cvt_pk_fp8_f32 v43, v26, v27
	v_pk_mul_f32 v[20:21], v[128:129], s[20:21] op_sel_hi:[1,0]
	v_pk_mul_f32 v[26:27], v[124:125], s[20:21] op_sel_hi:[1,0]
	v_cvt_pk_fp8_f32 v42, v20, v21 op_sel:[0,0,1]
	v_cvt_pk_fp8_f32 v43, v26, v27 op_sel:[0,0,1]
	v_pk_mul_f32 v[20:21], v[118:119], s[20:21] op_sel_hi:[1,0]
	v_pk_mul_f32 v[26:27], v[114:115], s[20:21] op_sel_hi:[1,0]
	v_cvt_pk_fp8_f32 v44, v20, v21
	v_cvt_pk_fp8_f32 v45, v26, v27
	v_add_u32_e32 v12, s31, v206
	v_ashrrev_i32_e32 v13, 31, v12
	v_pk_mul_f32 v[20:21], v[120:121], s[20:21] op_sel_hi:[1,0]
	v_pk_mul_f32 v[26:27], v[116:117], s[20:21] op_sel_hi:[1,0]
	v_or_b32_e32 v10, s84, v207
	v_lshlrev_b64 v[18:19], 11, v[12:13]
	v_cvt_pk_fp8_f32 v44, v20, v21 op_sel:[0,0,1]
	v_cvt_pk_fp8_f32 v45, v26, v27 op_sel:[0,0,1]
	v_ashrrev_i32_e32 v11, 31, v10
	v_lshl_add_u64 v[18:19], s[10:11], 0, v[18:19]
	v_lshl_add_u64 v[18:19], v[18:19], 0, v[10:11]
	s_nop 1
	v_permlane16_swap_b32 v42, v44
	v_permlane16_swap_b32 v43, v45
	v_and_b32_e32 v26, 1, v204
	v_mul_u32_u24_e32 v26, 0x78, v26
	v_mov_b32_e32 v27, 0
	v_lshl_add_u64 v[26:27], v[18:19], 0, v[26:27]
	global_store_dwordx4 v[26:27], v[42:45], off
	v_pk_mul_f32 v[20:21], v[110:111], s[20:21] op_sel_hi:[1,0]
	v_pk_mul_f32 v[26:27], v[106:107], s[20:21] op_sel_hi:[1,0]
	v_cvt_pk_fp8_f32 v46, v20, v21
	v_cvt_pk_fp8_f32 v47, v26, v27
	v_pk_mul_f32 v[20:21], v[112:113], s[20:21] op_sel_hi:[1,0]
	v_pk_mul_f32 v[26:27], v[108:109], s[20:21] op_sel_hi:[1,0]
	v_cvt_pk_fp8_f32 v46, v20, v21 op_sel:[0,0,1]
	v_cvt_pk_fp8_f32 v47, v26, v27 op_sel:[0,0,1]
	v_pk_mul_f32 v[20:21], v[102:103], s[20:21] op_sel_hi:[1,0]
	v_pk_mul_f32 v[26:27], v[98:99], s[20:21] op_sel_hi:[1,0]
	v_cvt_pk_fp8_f32 v48, v20, v21
	v_cvt_pk_fp8_f32 v49, v26, v27
	v_or_b32_e32 v18, 16, v12
	v_ashrrev_i32_e32 v19, 31, v18
	v_pk_mul_f32 v[20:21], v[104:105], s[20:21] op_sel_hi:[1,0]
	v_pk_mul_f32 v[26:27], v[100:101], s[20:21] op_sel_hi:[1,0]
	v_lshlrev_b64 v[18:19], 11, v[18:19]
	v_cvt_pk_fp8_f32 v48, v20, v21 op_sel:[0,0,1]
	v_cvt_pk_fp8_f32 v49, v26, v27 op_sel:[0,0,1]
	v_lshl_add_u64 v[18:19], s[10:11], 0, v[18:19]
	v_lshl_add_u64 v[18:19], v[18:19], 0, v[10:11]
	s_nop 1
	v_permlane16_swap_b32 v46, v48
	v_permlane16_swap_b32 v47, v49
	v_and_b32_e32 v26, 1, v204
	v_mul_u32_u24_e32 v26, 0x78, v26
	v_mov_b32_e32 v27, 0
	v_lshl_add_u64 v[26:27], v[18:19], 0, v[26:27]
	global_store_dwordx4 v[26:27], v[46:49], off
	v_pk_mul_f32 v[20:21], v[94:95], s[20:21] op_sel_hi:[1,0]
	v_pk_mul_f32 v[26:27], v[90:91], s[20:21] op_sel_hi:[1,0]
	v_cvt_pk_fp8_f32 v28, v20, v21
	v_cvt_pk_fp8_f32 v29, v26, v27
	v_pk_mul_f32 v[20:21], v[96:97], s[20:21] op_sel_hi:[1,0]
	v_pk_mul_f32 v[26:27], v[92:93], s[20:21] op_sel_hi:[1,0]
	v_cvt_pk_fp8_f32 v28, v20, v21 op_sel:[0,0,1]
	v_cvt_pk_fp8_f32 v29, v26, v27 op_sel:[0,0,1]
	v_pk_mul_f32 v[20:21], v[38:39], s[20:21] op_sel_hi:[1,0]
	v_pk_mul_f32 v[26:27], v[30:31], s[20:21] op_sel_hi:[1,0]
	v_cvt_pk_fp8_f32 v30, v20, v21
	v_cvt_pk_fp8_f32 v31, v26, v27
	v_or_b32_e32 v18, 32, v12
	v_ashrrev_i32_e32 v19, 31, v18
	v_pk_mul_f32 v[20:21], v[40:41], s[20:21] op_sel_hi:[1,0]
	v_pk_mul_f32 v[26:27], v[32:33], s[20:21] op_sel_hi:[1,0]
	v_lshlrev_b64 v[18:19], 11, v[18:19]
	v_cvt_pk_fp8_f32 v30, v20, v21 op_sel:[0,0,1]
	v_cvt_pk_fp8_f32 v31, v26, v27 op_sel:[0,0,1]
	v_lshl_add_u64 v[18:19], s[10:11], 0, v[18:19]
	v_lshl_add_u64 v[18:19], v[18:19], 0, v[10:11]
	s_nop 1
	v_permlane16_swap_b32 v28, v30
	v_permlane16_swap_b32 v29, v31
	v_and_b32_e32 v26, 1, v204
	v_mul_u32_u24_e32 v26, 0x78, v26
	v_mov_b32_e32 v27, 0
	v_lshl_add_u64 v[26:27], v[18:19], 0, v[26:27]
	global_store_dwordx4 v[26:27], v[28:31], off
	v_pk_mul_f32 v[18:19], v[22:23], s[20:21] op_sel_hi:[1,0]
	v_cvt_pk_fp8_f32 v20, v18, v19
	v_pk_mul_f32 v[14:15], v[14:15], s[20:21] op_sel_hi:[1,0]
	v_mov_b32_e32 v21, 0
	v_cvt_pk_fp8_f32 v21, v14, v15
	v_pk_mul_f32 v[14:15], v[24:25], s[20:21] op_sel_hi:[1,0]
	v_pk_mul_f32 v[6:7], v[6:7], s[20:21] op_sel_hi:[1,0]
	v_cvt_pk_fp8_f32 v20, v14, v15 op_sel:[0,0,1]
	v_pk_mul_f32 v[2:3], v[2:3], s[20:21] op_sel_hi:[1,0]
	v_cvt_pk_fp8_f32 v14, v6, v7
	v_cvt_pk_fp8_f32 v15, v2, v3
	v_or_b32_e32 v12, 48, v12
	v_pk_mul_f32 v[16:17], v[16:17], s[20:21] op_sel_hi:[1,0]
	v_ashrrev_i32_e32 v13, 31, v12
	v_cvt_pk_fp8_f32 v21, v16, v17 op_sel:[0,0,1]
	v_pk_mul_f32 v[2:3], v[8:9], s[20:21] op_sel_hi:[1,0]
	v_pk_mul_f32 v[4:5], v[4:5], s[20:21] op_sel_hi:[1,0]
	v_lshlrev_b64 v[12:13], 11, v[12:13]
	v_cvt_pk_fp8_f32 v14, v2, v3 op_sel:[0,0,1]
	v_cvt_pk_fp8_f32 v15, v4, v5 op_sel:[0,0,1]
	v_lshl_add_u64 v[2:3], s[10:11], 0, v[12:13]
	v_lshl_add_u64 v[2:3], v[2:3], 0, v[10:11]
	s_andn2_b64 vcc, exec, s[40:41]
	s_mov_b64 s[36:37], -1
	global_store_dwordx2 v[2:3], v[20:21], off
	global_store_dwordx2 v[2:3], v[14:15], off offset:128
	s_cbranch_vccnz .LBB0_1093
	s_andn2_b64 vcc, exec, s[8:9]
	s_cbranch_vccnz .LBB0_1092
	s_barrier
	s_branch .LBB0_1092

.LBB0_1954:
	s_lshl_b32 s2, s89, 7
	v_add_u32_e32 v142, s82, v205
	v_add_u32_e32 v158, s83, v205
	s_add_u32 s66, s40, s2
	ds_read_b128 v[130:133], v142
	ds_read_b128 v[134:137], v142 offset:1024
	ds_read_b128 v[138:141], v142 offset:2048
	ds_read_b128 v[142:145], v142 offset:3072
	ds_read_b128 v[146:149], v158
	ds_read_b128 v[150:153], v158 offset:1024
	ds_read_b128 v[154:157], v158 offset:2048
	ds_read_b128 v[158:161], v158 offset:3072
	s_addc_u32 s67, s41, 0
	s_add_u32 s68, s66, 0x100
	s_addc_u32 s69, s67, 0
	s_and_b64 s[66:67], s[62:63], exec
	s_cselect_b32 s67, s37, s69
	s_cselect_b32 s66, s85, s68
	s_add_i32 s70, s2, 0x100
	s_and_b64 s[68:69], s[62:63], exec
	s_cselect_b32 s70, 0, s70
	s_add_u32 s2, s38, s2
	s_addc_u32 s69, s39, 0
	s_add_u32 s68, s2, 0x20080
	s_addc_u32 s69, s69, 0
	v_lshl_add_u64 v[210:211], s[68:69], 0, v[194:195]
	s_add_i32 m0, s50, 0xc000
	ds_read_b128 v[162:165], v209
	ds_read_b128 v[166:169], v209 offset:1024
	ds_read_b128 v[170:173], v209 offset:2048
	ds_read_b128 v[174:177], v209 offset:3072
	ds_read_b128 v[178:181], v209 offset:4096
	ds_read_b128 v[182:185], v209 offset:5120
	ds_read_b128 v[186:189], v209 offset:6144
	ds_read_b128 v[190:193], v209 offset:7168
	global_load_lds_dwordx4 v[210:211], off
	v_lshl_add_u64 v[210:211], s[68:69], 0, v[198:199]
	s_add_i32 m0, s50, 0xe000
	s_nop 0
	global_load_lds_dwordx4 v[210:211], off
	s_waitcnt vmcnt(8)
	s_waitcnt lgkmcnt(0)
	s_barrier
	s_waitcnt lgkmcnt(0)
	v_mfma_f32_16x16x32_bf16 v[86:89], v[130:133], v[162:165], v[86:89]
	v_mfma_f32_16x16x32_bf16 v[82:85], v[138:141], v[162:165], v[82:85]
	v_mfma_f32_16x16x32_bf16 v[78:81], v[130:133], v[170:173], v[78:81]
	v_mfma_f32_16x16x32_bf16 v[74:77], v[138:141], v[170:173], v[74:77]
	v_mfma_f32_16x16x32_bf16 v[70:73], v[130:133], v[178:181], v[70:73]
	v_mfma_f32_16x16x32_bf16 v[66:69], v[138:141], v[178:181], v[66:69]
	v_mfma_f32_16x16x32_bf16 v[62:65], v[130:133], v[186:189], v[62:65]
	v_mfma_f32_16x16x32_bf16 v[58:61], v[138:141], v[186:189], v[58:61]
	v_mfma_f32_16x16x32_bf16 v[86:89], v[134:137], v[166:169], v[86:89]
	v_mfma_f32_16x16x32_bf16 v[82:85], v[142:145], v[166:169], v[82:85]
	v_mfma_f32_16x16x32_bf16 v[78:81], v[134:137], v[174:177], v[78:81]
	v_mfma_f32_16x16x32_bf16 v[74:77], v[142:145], v[174:177], v[74:77]
	v_mfma_f32_16x16x32_bf16 v[70:73], v[134:137], v[182:185], v[70:73]
	v_mfma_f32_16x16x32_bf16 v[66:69], v[142:145], v[182:185], v[66:69]
	v_mfma_f32_16x16x32_bf16 v[62:65], v[134:137], v[190:193], v[62:65]
	v_mfma_f32_16x16x32_bf16 v[58:61], v[142:145], v[190:193], v[58:61]
	v_mfma_f32_16x16x32_bf16 v[54:57], v[146:149], v[162:165], v[54:57]
	v_mfma_f32_16x16x32_bf16 v[50:53], v[154:157], v[162:165], v[50:53]
	v_mfma_f32_16x16x32_bf16 v[46:49], v[146:149], v[170:173], v[46:49]
	v_mfma_f32_16x16x32_bf16 v[42:45], v[154:157], v[170:173], v[42:45]
	v_mfma_f32_16x16x32_bf16 v[34:37], v[146:149], v[178:181], v[34:37]
	v_mfma_f32_16x16x32_bf16 v[30:33], v[154:157], v[178:181], v[30:33]
	v_mfma_f32_16x16x32_bf16 v[18:21], v[146:149], v[186:189], v[18:21]
	v_mfma_f32_16x16x32_bf16 v[14:17], v[154:157], v[186:189], v[14:17]
	v_mfma_f32_16x16x32_bf16 v[54:57], v[150:153], v[166:169], v[54:57]
	v_mfma_f32_16x16x32_bf16 v[50:53], v[158:161], v[166:169], v[50:53]
	v_mfma_f32_16x16x32_bf16 v[46:49], v[150:153], v[174:177], v[46:49]
	v_mfma_f32_16x16x32_bf16 v[42:45], v[158:161], v[174:177], v[42:45]
	v_mfma_f32_16x16x32_bf16 v[34:37], v[150:153], v[182:185], v[34:37]
	v_mfma_f32_16x16x32_bf16 v[30:33], v[158:161], v[182:185], v[30:33]
	v_mfma_f32_16x16x32_bf16 v[18:21], v[150:153], v[190:193], v[18:21]
	v_mfma_f32_16x16x32_bf16 v[14:17], v[158:161], v[190:193], v[14:17]
	s_barrier
	s_add_i32 s2, s82, s49
	v_lshl_add_u64 v[210:211], s[66:67], 0, v[196:197]
	s_mov_b32 m0, s2
	ds_read_b128 v[162:165], v209 offset:16384
	ds_read_b128 v[166:169], v209 offset:17408
	ds_read_b128 v[170:173], v209 offset:18432
	ds_read_b128 v[174:177], v209 offset:19456
	ds_read_b128 v[178:181], v209 offset:20480
	ds_read_b128 v[182:185], v209 offset:21504
	ds_read_b128 v[186:189], v209 offset:22528
	ds_read_b128 v[190:193], v209 offset:23552
	global_load_lds_dwordx4 v[210:211], off
	s_add_i32 m0, s2, 0x2000
	s_add_u32 s68, s66, 0x20000
	v_lshl_add_u64 v[212:213], s[66:67], 0, v[200:201]
	s_addc_u32 s69, s67, 0
	s_add_i32 s2, s83, s49
	global_load_lds_dwordx4 v[212:213], off
	v_lshl_add_u64 v[214:215], s[68:69], 0, v[196:197]
	s_mov_b32 m0, s2
	s_nop 0
	global_load_lds_dwordx4 v[214:215], off
	s_add_i32 m0, s2, 0x2000
	s_add_u32 s64, s64, s70
	v_lshl_add_u64 v[214:215], s[68:69], 0, v[200:201]
	s_addc_u32 s65, s65, 0
	global_load_lds_dwordx4 v[214:215], off
	v_lshl_add_u64 v[214:215], s[64:65], 0, v[194:195]
	s_mov_b32 m0, s50
	v_lshl_add_u64 v[216:217], s[64:65], 0, v[198:199]
	global_load_lds_dwordx4 v[214:215], off
	s_mov_b32 m0, s51
	s_nop 0
	global_load_lds_dwordx4 v[216:217], off
	s_waitcnt vmcnt(8)
	s_waitcnt lgkmcnt(0)
	s_barrier
	s_waitcnt lgkmcnt(0)
	v_mfma_f32_16x16x32_bf16 v[126:129], v[130:133], v[162:165], v[126:129]
	v_mfma_f32_16x16x32_bf16 v[122:125], v[138:141], v[162:165], v[122:125]
	v_mfma_f32_16x16x32_bf16 v[110:113], v[130:133], v[170:173], v[110:113]
	v_mfma_f32_16x16x32_bf16 v[106:109], v[138:141], v[170:173], v[106:109]
	v_mfma_f32_16x16x32_bf16 v[94:97], v[130:133], v[178:181], v[94:97]
	v_mfma_f32_16x16x32_bf16 v[90:93], v[138:141], v[178:181], v[90:93]
	v_mfma_f32_16x16x32_bf16 v[22:25], v[130:133], v[186:189], v[22:25]
	v_mfma_f32_16x16x32_bf16 v[10:13], v[138:141], v[186:189], v[10:13]
	v_mfma_f32_16x16x32_bf16 v[126:129], v[134:137], v[166:169], v[126:129]
	v_mfma_f32_16x16x32_bf16 v[122:125], v[142:145], v[166:169], v[122:125]
	v_mfma_f32_16x16x32_bf16 v[110:113], v[134:137], v[174:177], v[110:113]
	v_mfma_f32_16x16x32_bf16 v[106:109], v[142:145], v[174:177], v[106:109]
	v_mfma_f32_16x16x32_bf16 v[94:97], v[134:137], v[182:185], v[94:97]
	v_mfma_f32_16x16x32_bf16 v[90:93], v[142:145], v[182:185], v[90:93]
	v_mfma_f32_16x16x32_bf16 v[22:25], v[134:137], v[190:193], v[22:25]
	v_mfma_f32_16x16x32_bf16 v[10:13], v[142:145], v[190:193], v[10:13]
	v_mfma_f32_16x16x32_bf16 v[118:121], v[146:149], v[162:165], v[118:121]
	v_mfma_f32_16x16x32_bf16 v[114:117], v[154:157], v[162:165], v[114:117]
	v_mfma_f32_16x16x32_bf16 v[102:105], v[146:149], v[170:173], v[102:105]
	v_mfma_f32_16x16x32_bf16 v[98:101], v[154:157], v[170:173], v[98:101]
	v_mfma_f32_16x16x32_bf16 v[38:41], v[146:149], v[178:181], v[38:41]
	v_mfma_f32_16x16x32_bf16 v[26:29], v[154:157], v[178:181], v[26:29]
	v_mfma_f32_16x16x32_bf16 v[6:9], v[146:149], v[186:189], v[6:9]
	v_mfma_f32_16x16x32_bf16 v[2:5], v[154:157], v[186:189], v[2:5]
	v_mfma_f32_16x16x32_bf16 v[118:121], v[150:153], v[166:169], v[118:121]
	v_mfma_f32_16x16x32_bf16 v[114:117], v[158:161], v[166:169], v[114:117]
	v_mfma_f32_16x16x32_bf16 v[102:105], v[150:153], v[174:177], v[102:105]
	v_mfma_f32_16x16x32_bf16 v[98:101], v[158:161], v[174:177], v[98:101]
	v_mfma_f32_16x16x32_bf16 v[38:41], v[150:153], v[182:185], v[38:41]
	v_mfma_f32_16x16x32_bf16 v[26:29], v[158:161], v[182:185], v[26:29]
	v_mfma_f32_16x16x32_bf16 v[6:9], v[150:153], v[190:193], v[6:9]
	v_mfma_f32_16x16x32_bf16 v[2:5], v[158:161], v[190:193], v[2:5]
	s_barrier
	s_add_i32 s2, 0, 0x18000
	s_add_i32 s68, 0, 0x1c000
	v_add_u32_e32 v130, s2, v205
	v_add_u32_e32 v142, s68, v205
	ds_read_b128 v[146:149], v130
	ds_read_b128 v[150:153], v130 offset:1024
	ds_read_b128 v[154:157], v130 offset:2048
	ds_read_b128 v[158:161], v130 offset:3072
	ds_read_b128 v[130:133], v142
	ds_read_b128 v[134:137], v142 offset:1024
	ds_read_b128 v[138:141], v142 offset:2048
	ds_read_b128 v[142:145], v142 offset:3072
	s_add_u32 s64, s64, 0x20000
	s_addc_u32 s65, s65, 0
	s_mov_b32 m0, s52
	v_lshl_add_u64 v[218:219], s[64:65], 0, v[194:195]
	ds_read_b128 v[162:165], v209 offset:32768
	ds_read_b128 v[166:169], v209 offset:33792
	ds_read_b128 v[170:173], v209 offset:34816
	ds_read_b128 v[174:177], v209 offset:35840
	ds_read_b128 v[178:181], v209 offset:36864
	ds_read_b128 v[182:185], v209 offset:37888
	ds_read_b128 v[186:189], v209 offset:38912
	ds_read_b128 v[190:193], v209 offset:39936
	global_load_lds_dwordx4 v[218:219], off
	v_lshl_add_u64 v[218:219], s[64:65], 0, v[198:199]
	s_mov_b32 m0, s53
	s_nop 0
	global_load_lds_dwordx4 v[218:219], off
	s_waitcnt vmcnt(8)
	s_waitcnt lgkmcnt(0)
	s_barrier
	s_waitcnt lgkmcnt(0)
	v_mfma_f32_16x16x32_bf16 v[86:89], v[146:149], v[162:165], v[86:89]
	v_mfma_f32_16x16x32_bf16 v[82:85], v[154:157], v[162:165], v[82:85]
	v_mfma_f32_16x16x32_bf16 v[78:81], v[146:149], v[170:173], v[78:81]
	v_mfma_f32_16x16x32_bf16 v[74:77], v[154:157], v[170:173], v[74:77]
	v_mfma_f32_16x16x32_bf16 v[70:73], v[146:149], v[178:181], v[70:73]
	v_mfma_f32_16x16x32_bf16 v[66:69], v[154:157], v[178:181], v[66:69]
	v_mfma_f32_16x16x32_bf16 v[62:65], v[146:149], v[186:189], v[62:65]
	v_mfma_f32_16x16x32_bf16 v[58:61], v[154:157], v[186:189], v[58:61]
	v_mfma_f32_16x16x32_bf16 v[86:89], v[150:153], v[166:169], v[86:89]
	v_mfma_f32_16x16x32_bf16 v[82:85], v[158:161], v[166:169], v[82:85]
	v_mfma_f32_16x16x32_bf16 v[78:81], v[150:153], v[174:177], v[78:81]
	v_mfma_f32_16x16x32_bf16 v[74:77], v[158:161], v[174:177], v[74:77]
	v_mfma_f32_16x16x32_bf16 v[70:73], v[150:153], v[182:185], v[70:73]
	v_mfma_f32_16x16x32_bf16 v[66:69], v[158:161], v[182:185], v[66:69]
	v_mfma_f32_16x16x32_bf16 v[62:65], v[150:153], v[190:193], v[62:65]
	v_mfma_f32_16x16x32_bf16 v[58:61], v[158:161], v[190:193], v[58:61]
	v_mfma_f32_16x16x32_bf16 v[54:57], v[130:133], v[162:165], v[54:57]
	v_mfma_f32_16x16x32_bf16 v[50:53], v[138:141], v[162:165], v[50:53]
	v_mfma_f32_16x16x32_bf16 v[46:49], v[130:133], v[170:173], v[46:49]
	v_mfma_f32_16x16x32_bf16 v[42:45], v[138:141], v[170:173], v[42:45]
	v_mfma_f32_16x16x32_bf16 v[34:37], v[130:133], v[178:181], v[34:37]
	v_mfma_f32_16x16x32_bf16 v[30:33], v[138:141], v[178:181], v[30:33]
	v_mfma_f32_16x16x32_bf16 v[18:21], v[130:133], v[186:189], v[18:21]
	v_mfma_f32_16x16x32_bf16 v[14:17], v[138:141], v[186:189], v[14:17]
	v_mfma_f32_16x16x32_bf16 v[54:57], v[134:137], v[166:169], v[54:57]
	v_mfma_f32_16x16x32_bf16 v[50:53], v[142:145], v[166:169], v[50:53]
	v_mfma_f32_16x16x32_bf16 v[46:49], v[134:137], v[174:177], v[46:49]
	v_mfma_f32_16x16x32_bf16 v[42:45], v[142:145], v[174:177], v[42:45]
	v_mfma_f32_16x16x32_bf16 v[34:37], v[134:137], v[182:185], v[34:37]
	v_mfma_f32_16x16x32_bf16 v[30:33], v[142:145], v[182:185], v[30:33]
	v_mfma_f32_16x16x32_bf16 v[18:21], v[134:137], v[190:193], v[18:21]
	v_mfma_f32_16x16x32_bf16 v[14:17], v[142:145], v[190:193], v[14:17]
	s_barrier
	s_add_i32 s2, s2, s49
	v_lshl_add_u64 v[210:211], v[210:211], 0, s[12:13]
	s_mov_b32 m0, s2
	ds_read_b128 v[186:189], v209 offset:49152
	ds_read_b128 v[190:193], v209 offset:50176
	ds_read_b128 v[178:181], v209 offset:51200
	ds_read_b128 v[182:185], v209 offset:52224
	ds_read_b128 v[170:173], v209 offset:53248
	ds_read_b128 v[174:177], v209 offset:54272
	ds_read_b128 v[162:165], v209 offset:55296
	ds_read_b128 v[166:169], v209 offset:56320
	global_load_lds_dwordx4 v[210:211], off
	s_add_i32 m0, s2, 0x2000
	s_add_u32 s64, s66, 0x20080
	v_lshl_add_u64 v[210:211], v[212:213], 0, s[12:13]
	s_addc_u32 s65, s67, 0
	s_add_i32 s2, s68, s49
	global_load_lds_dwordx4 v[210:211], off
	v_lshl_add_u64 v[210:211], s[64:65], 0, v[196:197]
	s_mov_b32 m0, s2
	s_andn2_b64 vcc, exec, s[62:63]
	global_load_lds_dwordx4 v[210:211], off
	v_lshl_add_u64 v[210:211], s[64:65], 0, v[200:201]
	s_add_i32 m0, s2, 0x2000
	s_nop 0
	global_load_lds_dwordx4 v[210:211], off
	v_lshl_add_u64 v[210:211], v[214:215], 0, s[12:13]
	s_mov_b32 m0, s75
	s_nop 0
	global_load_lds_dwordx4 v[210:211], off
	v_lshl_add_u64 v[210:211], v[216:217], 0, s[12:13]
	s_mov_b32 m0, s76
	s_nop 0
	global_load_lds_dwordx4 v[210:211], off
	s_waitcnt vmcnt(8)
	s_waitcnt lgkmcnt(0)
	s_barrier
	s_cbranch_vccnz .LBB0_1936
	v_pk_mul_f32 v[214:215], v[86:87], s[20:21] op_sel_hi:[1,0]
	v_pk_mul_f32 v[216:217], v[82:83], s[20:21] op_sel_hi:[1,0]
	v_cvt_pk_fp8_f32 v218, v214, v215
	v_cvt_pk_fp8_f32 v219, v216, v217
	v_pk_mul_f32 v[214:215], v[88:89], s[20:21] op_sel_hi:[1,0]
	v_pk_mul_f32 v[216:217], v[84:85], s[20:21] op_sel_hi:[1,0]
	v_cvt_pk_fp8_f32 v218, v214, v215 op_sel:[0,0,1]
	v_cvt_pk_fp8_f32 v219, v216, v217 op_sel:[0,0,1]
	v_pk_mul_f32 v[214:215], v[54:55], s[20:21] op_sel_hi:[1,0]
	v_pk_mul_f32 v[216:217], v[50:51], s[20:21] op_sel_hi:[1,0]
	v_mov_b32_e32 v210, v1
	v_mov_b32_e32 v211, v204
	v_cvt_pk_fp8_f32 v220, v214, v215
	v_cvt_pk_fp8_f32 v221, v216, v217
	v_pk_mul_f32 v[214:215], v[56:57], s[20:21] op_sel_hi:[1,0]
	v_add_u32_e32 v210, s87, v210
	v_lshl_add_u32 v212, v211, 3, s88
	v_ashrrev_i32_e32 v211, 31, v210
	v_pk_mul_f32 v[216:217], v[52:53], s[20:21] op_sel_hi:[1,0]
	v_lshlrev_b64 v[210:211], 11, v[210:211]
	v_cvt_pk_fp8_f32 v220, v214, v215 op_sel:[0,0,1]
	v_cvt_pk_fp8_f32 v221, v216, v217 op_sel:[0,0,1]
	v_ashrrev_i32_e32 v213, 31, v212
	v_lshl_add_u64 v[210:211], s[10:11], 0, v[210:211]
	v_lshl_add_u64 v[210:211], v[210:211], 0, v[212:213]
	s_nop 1
	v_permlane16_swap_b32 v218, v220
	v_permlane16_swap_b32 v219, v221
	v_and_b32_e32 v216, 1, v204
	v_mul_u32_u24_e32 v216, 0x78, v216
	v_mov_b32_e32 v217, 0
	v_lshl_add_u64 v[216:217], v[210:211], 0, v[216:217]
	global_store_dwordx4 v[216:217], v[218:221], off
	v_pk_mul_f32 v[214:215], v[78:79], s[20:21] op_sel_hi:[1,0]
	v_pk_mul_f32 v[216:217], v[74:75], s[20:21] op_sel_hi:[1,0]
	v_cvt_pk_fp8_f32 v218, v214, v215
	v_cvt_pk_fp8_f32 v219, v216, v217
	v_pk_mul_f32 v[214:215], v[80:81], s[20:21] op_sel_hi:[1,0]
	v_pk_mul_f32 v[216:217], v[76:77], s[20:21] op_sel_hi:[1,0]
	v_cvt_pk_fp8_f32 v218, v214, v215 op_sel:[0,0,1]
	v_cvt_pk_fp8_f32 v219, v216, v217 op_sel:[0,0,1]
	v_pk_mul_f32 v[214:215], v[46:47], s[20:21] op_sel_hi:[1,0]
	v_pk_mul_f32 v[216:217], v[42:43], s[20:21] op_sel_hi:[1,0]
	v_cvt_pk_fp8_f32 v220, v214, v215
	v_cvt_pk_fp8_f32 v221, v216, v217
	v_pk_mul_f32 v[214:215], v[48:49], s[20:21] op_sel_hi:[1,0]
	v_pk_mul_f32 v[216:217], v[44:45], s[20:21] op_sel_hi:[1,0]
	v_cvt_pk_fp8_f32 v220, v214, v215 op_sel:[0,0,1]
	v_cvt_pk_fp8_f32 v221, v216, v217 op_sel:[0,0,1]
	s_mov_b32 s2, 0x8000
	v_add_co_u32_e32 v214, vcc, s2, v210
	v_lshl_add_u64 v[212:213], v[210:211], 0, s[24:25]
	s_nop 0
	v_addc_co_u32_e32 v215, vcc, 0, v211, vcc
	s_nop 1
	v_permlane16_swap_b32 v218, v220
	v_permlane16_swap_b32 v219, v221
	v_and_b32_e32 v216, 1, v204
	v_mul_u32_u24_e32 v216, 0x78, v216
	v_mov_b32_e32 v217, 0
	v_lshl_add_u64 v[216:217], v[214:215], 0, v[216:217]
	global_store_dwordx4 v[216:217], v[218:221], off
	v_pk_mul_f32 v[214:215], v[70:71], s[20:21] op_sel_hi:[1,0]
	v_pk_mul_f32 v[216:217], v[66:67], s[20:21] op_sel_hi:[1,0]
	v_cvt_pk_fp8_f32 v218, v214, v215
	v_cvt_pk_fp8_f32 v219, v216, v217
	v_pk_mul_f32 v[214:215], v[72:73], s[20:21] op_sel_hi:[1,0]
	v_pk_mul_f32 v[216:217], v[68:69], s[20:21] op_sel_hi:[1,0]
	v_cvt_pk_fp8_f32 v218, v214, v215 op_sel:[0,0,1]
	v_cvt_pk_fp8_f32 v219, v216, v217 op_sel:[0,0,1]
	v_pk_mul_f32 v[214:215], v[34:35], s[20:21] op_sel_hi:[1,0]
	v_pk_mul_f32 v[216:217], v[30:31], s[20:21] op_sel_hi:[1,0]
	v_cvt_pk_fp8_f32 v220, v214, v215
	v_cvt_pk_fp8_f32 v221, v216, v217
	v_pk_mul_f32 v[214:215], v[36:37], s[20:21] op_sel_hi:[1,0]
	v_pk_mul_f32 v[216:217], v[32:33], s[20:21] op_sel_hi:[1,0]
	v_cvt_pk_fp8_f32 v220, v214, v215 op_sel:[0,0,1]
	v_cvt_pk_fp8_f32 v221, v216, v217 op_sel:[0,0,1]
	s_mov_b32 s2, 0x10000
	v_add_co_u32_e32 v214, vcc, s2, v210
	v_lshl_add_u64 v[212:213], v[210:211], 0, s[28:29]
	s_nop 0
	v_addc_co_u32_e32 v215, vcc, 0, v211, vcc
	s_nop 1
	v_permlane16_swap_b32 v218, v220
	v_permlane16_swap_b32 v219, v221
	v_and_b32_e32 v216, 1, v204
	v_mul_u32_u24_e32 v216, 0x78, v216
	v_mov_b32_e32 v217, 0
	v_lshl_add_u64 v[216:217], v[214:215], 0, v[216:217]
	global_store_dwordx4 v[216:217], v[218:221], off
	v_pk_mul_f32 v[214:215], v[62:63], s[20:21] op_sel_hi:[1,0]
	v_pk_mul_f32 v[216:217], v[58:59], s[20:21] op_sel_hi:[1,0]
	v_cvt_pk_fp8_f32 v218, v214, v215
	v_cvt_pk_fp8_f32 v219, v216, v217
	v_pk_mul_f32 v[214:215], v[64:65], s[20:21] op_sel_hi:[1,0]
	v_pk_mul_f32 v[216:217], v[60:61], s[20:21] op_sel_hi:[1,0]
	v_cvt_pk_fp8_f32 v218, v214, v215 op_sel:[0,0,1]
	v_cvt_pk_fp8_f32 v219, v216, v217 op_sel:[0,0,1]
	v_pk_mul_f32 v[214:215], v[18:19], s[20:21] op_sel_hi:[1,0]
	v_pk_mul_f32 v[216:217], v[14:15], s[20:21] op_sel_hi:[1,0]
	v_cvt_pk_fp8_f32 v220, v214, v215
	v_cvt_pk_fp8_f32 v221, v216, v217
	v_pk_mul_f32 v[214:215], v[20:21], s[20:21] op_sel_hi:[1,0]
	v_pk_mul_f32 v[216:217], v[16:17], s[20:21] op_sel_hi:[1,0]
	v_cvt_pk_fp8_f32 v220, v214, v215 op_sel:[0,0,1]
	v_cvt_pk_fp8_f32 v221, v216, v217 op_sel:[0,0,1]
	s_mov_b32 s2, 0x18000
	v_lshl_add_u64 v[212:213], v[210:211], 0, s[30:31]
	v_add_co_u32_e32 v210, vcc, s2, v210
	s_nop 1
	v_addc_co_u32_e32 v211, vcc, 0, v211, vcc
	s_nop 1
	v_permlane16_swap_b32 v218, v220
	v_permlane16_swap_b32 v219, v221
	v_and_b32_e32 v216, 1, v204
	v_mul_u32_u24_e32 v216, 0x78, v216
	v_mov_b32_e32 v217, 0
	v_lshl_add_u64 v[216:217], v[210:211], 0, v[216:217]
	global_store_dwordx4 v[216:217], v[218:221], off
	s_branch .LBB0_1936

.LBB0_1958:
	v_pk_mul_f32 v[20:21], v[126:127], s[20:21] op_sel_hi:[1,0]
	v_pk_mul_f32 v[30:31], v[122:123], s[20:21] op_sel_hi:[1,0]
	v_cvt_pk_fp8_f32 v32, v20, v21
	v_cvt_pk_fp8_f32 v33, v30, v31
	v_pk_mul_f32 v[20:21], v[128:129], s[20:21] op_sel_hi:[1,0]
	v_pk_mul_f32 v[30:31], v[124:125], s[20:21] op_sel_hi:[1,0]
	v_cvt_pk_fp8_f32 v32, v20, v21 op_sel:[0,0,1]
	v_cvt_pk_fp8_f32 v33, v30, v31 op_sel:[0,0,1]
	v_pk_mul_f32 v[20:21], v[118:119], s[20:21] op_sel_hi:[1,0]
	v_pk_mul_f32 v[30:31], v[114:115], s[20:21] op_sel_hi:[1,0]
	v_cvt_pk_fp8_f32 v34, v20, v21
	v_cvt_pk_fp8_f32 v35, v30, v31
	v_add_u32_e32 v16, s35, v206
	v_ashrrev_i32_e32 v17, 31, v16
	v_pk_mul_f32 v[20:21], v[120:121], s[20:21] op_sel_hi:[1,0]
	v_pk_mul_f32 v[30:31], v[116:117], s[20:21] op_sel_hi:[1,0]
	v_or_b32_e32 v14, s86, v207
	v_lshlrev_b64 v[18:19], 11, v[16:17]
	v_cvt_pk_fp8_f32 v34, v20, v21 op_sel:[0,0,1]
	v_cvt_pk_fp8_f32 v35, v30, v31 op_sel:[0,0,1]
	v_ashrrev_i32_e32 v15, 31, v14
	v_lshl_add_u64 v[18:19], s[10:11], 0, v[18:19]
	v_lshl_add_u64 v[18:19], v[18:19], 0, v[14:15]
	s_nop 1
	v_permlane16_swap_b32 v32, v34
	v_permlane16_swap_b32 v33, v35
	v_and_b32_e32 v30, 1, v204
	v_mul_u32_u24_e32 v30, 0x78, v30
	v_mov_b32_e32 v31, 0
	v_lshl_add_u64 v[30:31], v[18:19], 0, v[30:31]
	global_store_dwordx4 v[30:31], v[32:35], off
	v_pk_mul_f32 v[20:21], v[110:111], s[20:21] op_sel_hi:[1,0]
	v_pk_mul_f32 v[30:31], v[106:107], s[20:21] op_sel_hi:[1,0]
	v_cvt_pk_fp8_f32 v32, v20, v21
	v_cvt_pk_fp8_f32 v33, v30, v31
	v_pk_mul_f32 v[20:21], v[112:113], s[20:21] op_sel_hi:[1,0]
	v_pk_mul_f32 v[30:31], v[108:109], s[20:21] op_sel_hi:[1,0]
	v_cvt_pk_fp8_f32 v32, v20, v21 op_sel:[0,0,1]
	v_cvt_pk_fp8_f32 v33, v30, v31 op_sel:[0,0,1]
	v_pk_mul_f32 v[20:21], v[102:103], s[20:21] op_sel_hi:[1,0]
	v_pk_mul_f32 v[30:31], v[98:99], s[20:21] op_sel_hi:[1,0]
	v_cvt_pk_fp8_f32 v34, v20, v21
	v_cvt_pk_fp8_f32 v35, v30, v31
	v_or_b32_e32 v18, 16, v16
	v_ashrrev_i32_e32 v19, 31, v18
	v_pk_mul_f32 v[20:21], v[104:105], s[20:21] op_sel_hi:[1,0]
	v_pk_mul_f32 v[30:31], v[100:101], s[20:21] op_sel_hi:[1,0]
	v_lshlrev_b64 v[18:19], 11, v[18:19]
	v_cvt_pk_fp8_f32 v34, v20, v21 op_sel:[0,0,1]
	v_cvt_pk_fp8_f32 v35, v30, v31 op_sel:[0,0,1]
	v_lshl_add_u64 v[18:19], s[10:11], 0, v[18:19]
	v_lshl_add_u64 v[18:19], v[18:19], 0, v[14:15]
	s_nop 1
	v_permlane16_swap_b32 v32, v34
	v_permlane16_swap_b32 v33, v35
	v_and_b32_e32 v30, 1, v204
	v_mul_u32_u24_e32 v30, 0x78, v30
	v_mov_b32_e32 v31, 0
	v_lshl_add_u64 v[30:31], v[18:19], 0, v[30:31]
	global_store_dwordx4 v[30:31], v[32:35], off
	v_pk_mul_f32 v[20:21], v[94:95], s[20:21] op_sel_hi:[1,0]
	v_pk_mul_f32 v[30:31], v[90:91], s[20:21] op_sel_hi:[1,0]
	v_cvt_pk_fp8_f32 v46, v20, v21
	v_cvt_pk_fp8_f32 v47, v30, v31
	v_pk_mul_f32 v[20:21], v[96:97], s[20:21] op_sel_hi:[1,0]
	v_pk_mul_f32 v[30:31], v[92:93], s[20:21] op_sel_hi:[1,0]
	v_cvt_pk_fp8_f32 v46, v20, v21 op_sel:[0,0,1]
	v_cvt_pk_fp8_f32 v47, v30, v31 op_sel:[0,0,1]
	v_pk_mul_f32 v[20:21], v[38:39], s[20:21] op_sel_hi:[1,0]
	v_pk_mul_f32 v[26:27], v[26:27], s[20:21] op_sel_hi:[1,0]
	v_cvt_pk_fp8_f32 v48, v20, v21
	v_cvt_pk_fp8_f32 v49, v26, v27
	v_or_b32_e32 v18, 32, v16
	v_ashrrev_i32_e32 v19, 31, v18
	v_pk_mul_f32 v[20:21], v[40:41], s[20:21] op_sel_hi:[1,0]
	v_pk_mul_f32 v[26:27], v[28:29], s[20:21] op_sel_hi:[1,0]
	v_lshlrev_b64 v[18:19], 11, v[18:19]
	v_cvt_pk_fp8_f32 v48, v20, v21 op_sel:[0,0,1]
	v_cvt_pk_fp8_f32 v49, v26, v27 op_sel:[0,0,1]
	v_lshl_add_u64 v[18:19], s[10:11], 0, v[18:19]
	v_lshl_add_u64 v[18:19], v[18:19], 0, v[14:15]
	s_nop 1
	v_permlane16_swap_b32 v46, v48
	v_permlane16_swap_b32 v47, v49
	v_and_b32_e32 v26, 1, v204
	v_mul_u32_u24_e32 v26, 0x78, v26
	v_mov_b32_e32 v27, 0
	v_lshl_add_u64 v[26:27], v[18:19], 0, v[26:27]
	global_store_dwordx4 v[26:27], v[46:49], off
	v_pk_mul_f32 v[18:19], v[22:23], s[20:21] op_sel_hi:[1,0]
	v_cvt_pk_fp8_f32 v20, v18, v19
	v_pk_mul_f32 v[10:11], v[10:11], s[20:21] op_sel_hi:[1,0]
	v_mov_b32_e32 v21, 0
	v_cvt_pk_fp8_f32 v21, v10, v11
	v_pk_mul_f32 v[10:11], v[24:25], s[20:21] op_sel_hi:[1,0]
	v_pk_mul_f32 v[6:7], v[6:7], s[20:21] op_sel_hi:[1,0]
	v_cvt_pk_fp8_f32 v20, v10, v11 op_sel:[0,0,1]
	v_pk_mul_f32 v[2:3], v[2:3], s[20:21] op_sel_hi:[1,0]
	v_cvt_pk_fp8_f32 v10, v6, v7
	v_cvt_pk_fp8_f32 v11, v2, v3
	v_or_b32_e32 v16, 48, v16
	v_pk_mul_f32 v[12:13], v[12:13], s[20:21] op_sel_hi:[1,0]
	v_ashrrev_i32_e32 v17, 31, v16
	v_cvt_pk_fp8_f32 v21, v12, v13 op_sel:[0,0,1]
	v_pk_mul_f32 v[2:3], v[8:9], s[20:21] op_sel_hi:[1,0]
	v_pk_mul_f32 v[4:5], v[4:5], s[20:21] op_sel_hi:[1,0]
	v_lshlrev_b64 v[16:17], 11, v[16:17]
	v_cvt_pk_fp8_f32 v10, v2, v3 op_sel:[0,0,1]
	v_cvt_pk_fp8_f32 v11, v4, v5 op_sel:[0,0,1]
	v_lshl_add_u64 v[2:3], s[10:11], 0, v[16:17]
	v_lshl_add_u64 v[2:3], v[2:3], 0, v[14:15]
	s_andn2_b64 vcc, exec, s[54:55]
	s_mov_b64 s[38:39], -1
	global_store_dwordx2 v[2:3], v[20:21], off
	global_store_dwordx2 v[2:3], v[10:11], off offset:128
	s_cbranch_vccnz .LBB0_1925
	s_andn2_b64 vcc, exec, s[8:9]
	s_cbranch_vccnz .LBB0_1924
	s_barrier
	s_branch .LBB0_1924
